# speedup vs baseline: 1.0066x; 1.0066x over previous
.LBB2_6:
	s_or_b64 exec, exec, s[18:19]
	v_xor_b32_e32 v23, 32, v23
	s_add_i32 s38, 0, 0x1c000
	v_lshlrev_b32_e32 v23, 2, v23
	v_lshlrev_b32_e32 v199, 2, v25
	s_waitcnt vmcnt(4) lgkmcnt(0)
	s_barrier
	v_add3_u32 v23, s38, v23, v199
	ds_read_b32 v23, v23
	v_max_f32_e32 v24, v24, v24
	v_mul_f32_e32 v22, 0x3db8aa3b, v22
	v_mov_b32_e32 v164, 0
	v_mov_b32_e32 v165, 0
	s_waitcnt lgkmcnt(0)
	s_movk_i32 s45, 0x4000
	v_add3_u32 v250, s45, v184, v185
	v_add3_u32 v251, s45, v184, v186
	v_add3_u32 v252, s45, v184, v187
	v_add3_u32 v253, s45, v184, v188
	ds_read_b128 v[218:221], v250 offset:49152
	ds_read_b128 v[222:225], v251 offset:49152
	ds_read_b128 v[242:245], v252 offset:49152
	ds_read_b128 v[246:249], v253 offset:49152
	v_add3_u32 v250, s45, v184, v189
	v_add3_u32 v251, s45, v184, v190
	v_add3_u32 v252, s45, v184, v191
	v_add3_u32 v253, s45, v184, v192
	ds_read_b128 v[202:205], v250 offset:49152
	ds_read_b128 v[206:209], v251 offset:49152
	ds_read_b128 v[210:213], v252 offset:49152
	ds_read_b128 v[214:217], v253 offset:49152
	v_max_f32_e32 v23, v23, v23
	v_max_f32_e32 v197, v24, v23
	v_mov_b32_e32 v23, 2.0
	v_fmamk_f32 v200, v197, 0xbdb8aa3b, v23
	v_fmamk_f32 v23, v22, 0xcb400000, v200
	v_fma_f32 v2, v2, v22, v23
	v_fma_f32 v3, v3, v22, v23
	v_fma_f32 v6, v6, v22, v23
	v_fma_f32 v7, v7, v22, v23
	v_fma_f32 v10, v10, v22, v23
	v_fma_f32 v11, v11, v22, v23
	v_fma_f32 v14, v14, v22, v23
	v_fma_f32 v15, v15, v22, v23
	v_exp_f32_e32 v2, v2
	v_exp_f32_e32 v3, v3
	v_exp_f32_e32 v6, v6
	v_exp_f32_e32 v7, v7
	v_exp_f32_e32 v10, v10
	v_exp_f32_e32 v11, v11
	v_exp_f32_e32 v14, v14
	v_exp_f32_e32 v15, v15
	v_fma_f32 v4, v4, v22, v23
	v_fma_f32 v5, v5, v22, v23
	v_fma_f32 v8, v8, v22, v23
	v_fma_f32 v9, v9, v22, v23
	v_fma_f32 v12, v12, v22, v23
	v_fma_f32 v13, v13, v22, v23
	v_fma_f32 v16, v16, v22, v23
	v_fmac_f32_e32 v23, v17, v22
	v_mov_b32_e32 v166, 0
	v_mov_b32_e32 v167, 0
	v_exp_f32_e32 v4, v4
	v_exp_f32_e32 v5, v5
	v_exp_f32_e32 v8, v8
	v_exp_f32_e32 v9, v9
	v_exp_f32_e32 v12, v12
	v_exp_f32_e32 v13, v13
	v_exp_f32_e32 v16, v16
	v_exp_f32_e32 v17, v23
	v_add_f32_e32 v250, v2, v3
	v_add_f32_e32 v251, v4, v5
	v_add_f32_e32 v252, v6, v7
	v_add_f32_e32 v253, v8, v9
	v_add_f32_e32 v250, v250, v251
	v_add_f32_e32 v252, v252, v253
	v_add_f32_e32 v251, v10, v11
	v_add_f32_e32 v253, v12, v13
	v_add_f32_e32 v250, v250, v252
	v_add_f32_e32 v251, v251, v253
	v_add_f32_e32 v252, v14, v15
	v_add_f32_e32 v253, v16, v17
	v_add_f32_e32 v250, v250, v251
	v_add_f32_e32 v252, v252, v253
	v_add_f32_e32 v250, v250, v252
	v_cvt_pk_fp8_f32 v164, v2, v3
	v_cvt_pk_fp8_f32 v165, v6, v7
	v_cvt_pk_fp8_f32 v166, v10, v11
	v_cvt_pk_fp8_f32 v167, v14, v15
	s_lshl_b32 s0, s22, 11
	s_add_i32 s0, s0, 0
	s_add_i32 s0, s0, 0x18000
	v_cvt_pk_fp8_f32 v164, v4, v5 op_sel:[0,0,1]
	v_cvt_pk_fp8_f32 v165, v8, v9 op_sel:[0,0,1]
	v_cvt_pk_fp8_f32 v166, v12, v13 op_sel:[0,0,1]
	v_cvt_pk_fp8_f32 v167, v16, v17 op_sel:[0,0,1]
	v_lshl_add_u32 v193, v198, 4, s0
	v_lshrrev_b32_e32 v3, 2, v0
	v_lshlrev_b32_e32 v6, 1, v183
	s_lshl_b32 s0, s20, 20
	v_bfe_u32 v4, v0, 2, 2
	v_lshl_or_b32 v5, v1, 6, s24
	v_bitop3_b32 v3, v6, v3, 3 bitop3:0x78
	s_or_b32 s18, s0, s23
	v_lshl_add_u32 v194, s34, 10, v193
	v_lshl_or_b32 v195, v3, 4, v5
	v_bitop3_b32 v3, v6, v4, 1 bitop3:0x36
	v_add3_u32 v4, s21, v20, v21
	s_add_u32 s0, s6, s18
	ds_write_b128 v194, v[164:167]
	v_lshl_or_b32 v196, v3, 4, v5
	v_ashrrev_i32_e32 v5, 31, v4
	s_addc_u32 s1, s7, 0
	s_waitcnt vmcnt(2) lgkmcnt(0)
	s_barrier
	s_mov_b64 s[60:61], s[0:1]
	v_lshl_add_u64 v[170:171], s[0:1], 0, v[4:5]
	v_add3_u32 v4, s21, v18, v19
	s_add_u32 s0, s8, s18
	v_mov_b32_e32 v2, 0
	v_ashrrev_i32_e32 v5, 31, v4
	s_addc_u32 s1, s9, 0
	s_mov_b32 s39, 0
	s_mov_b32 s40, 1
	s_mov_b64 s[64:65], s[0:1]
	v_lshl_add_u64 v[172:173], s[0:1], 0, v[4:5]
	s_mov_b64 s[6:7], 0
	s_movk_i32 s41, 0x2000
	s_mov_b64 s[8:9], 0xc000
	s_mov_b64 s[18:19], 0xe000
	s_mov_b64 s[20:21], 0x8000
	s_mov_b64 s[22:23], 0xa000
	s_mov_b32 s42, 0x42966666
	v_mov_b32_e32 v82, 0x4b400000
	v_mov_b32_e32 v100, 0x38383838
	s_mov_b32 s0, 0
	s_mov_b32 s43, 1
	v_mov_b32_e32 v3, v2
	v_mov_b32_e32 v4, v2
	v_mov_b32_e32 v5, v2
	v_mov_b32_e32 v6, v2
	v_mov_b32_e32 v7, v2
	v_mov_b32_e32 v8, v2
	v_mov_b32_e32 v9, v2
	v_mov_b32_e32 v10, v2
	v_mov_b32_e32 v11, v2
	v_mov_b32_e32 v12, v2
	v_mov_b32_e32 v13, v2
	v_mov_b32_e32 v14, v2
	v_mov_b32_e32 v15, v2
	v_mov_b32_e32 v16, v2
	v_mov_b32_e32 v17, v2
	v_mov_b32_e32 v18, v2
	v_mov_b32_e32 v19, v2
	v_mov_b32_e32 v20, v2
	v_mov_b32_e32 v21, v2
	v_mov_b32_e32 v22, v2
	v_mov_b32_e32 v23, v2
	v_mov_b32_e32 v24, v2
	v_mov_b32_e32 v25, v2
	v_mov_b32_e32 v26, v2
	v_mov_b32_e32 v27, v2
	v_mov_b32_e32 v28, v2
	v_mov_b32_e32 v29, v2
	v_mov_b32_e32 v30, v2
	v_mov_b32_e32 v31, v2
	v_mov_b32_e32 v32, v2
	v_mov_b32_e32 v33, v2
	v_mov_b32_e32 v34, v2
	v_mov_b32_e32 v35, v2
	v_mov_b32_e32 v36, v2
	v_mov_b32_e32 v37, v2
	v_mov_b32_e32 v38, v2
	v_mov_b32_e32 v39, v2
	v_mov_b32_e32 v40, v2
	v_mov_b32_e32 v41, v2
	v_mov_b32_e32 v42, v2
	v_mov_b32_e32 v43, v2
	v_mov_b32_e32 v44, v2
	v_mov_b32_e32 v45, v2
	v_mov_b32_e32 v46, v2
	v_mov_b32_e32 v47, v2
	v_mov_b32_e32 v48, v2
	v_mov_b32_e32 v49, v2
	v_mov_b32_e32 v50, v2
	v_mov_b32_e32 v51, v2
	v_mov_b32_e32 v52, v2
	v_mov_b32_e32 v53, v2
	v_mov_b32_e32 v54, v2
	v_mov_b32_e32 v55, v2
	v_mov_b32_e32 v56, v2
	v_mov_b32_e32 v57, v2
	v_mov_b32_e32 v58, v2
	v_mov_b32_e32 v59, v2
	v_mov_b32_e32 v60, v2
	v_mov_b32_e32 v61, v2
	v_mov_b32_e32 v62, v2
	v_mov_b32_e32 v63, v2
	v_mov_b32_e32 v64, v2
	v_mov_b32_e32 v65, v2
	v_mov_b32_e32 v66, v2
	v_mov_b32_e32 v67, v2
	v_mov_b32_e32 v68, v2
	v_mov_b32_e32 v69, v2
	v_mov_b32_e32 v70, v2
	v_mov_b32_e32 v71, v2
	v_mov_b32_e32 v72, v2
	v_mov_b32_e32 v73, v2
	v_mov_b32_e32 v74, v2
	v_mov_b32_e32 v75, v2
	v_mov_b32_e32 v76, v2
	v_mov_b32_e32 v77, v2
	v_mov_b32_e32 v78, v2
	v_mov_b32_e32 v79, v2
	v_mov_b32_e32 v80, v2
	v_mov_b32_e32 v81, v2
	v_mov_b32_e32 v66, v250
	v_mov_b32_e32 v226, 0x4b400000
	v_mov_b32_e32 v227, v226
	v_mov_b32_e32 v228, v226
	v_mov_b32_e32 v229, v226
	v_mov_b32_e32 v230, v226
	v_mov_b32_e32 v231, v226
	v_mov_b32_e32 v232, v226
	v_mov_b32_e32 v233, v226
	v_mov_b32_e32 v234, v226
	v_mov_b32_e32 v235, v226
	v_mov_b32_e32 v236, v226
	v_mov_b32_e32 v237, v226
	v_mov_b32_e32 v238, v226
	v_mov_b32_e32 v239, v226
	v_mov_b32_e32 v240, v226
	v_mov_b32_e32 v241, v226
	v_add_u32_e32 v250, 0xc000, v184
	v_add_u32_e32 v185, v185, v250
	v_add_u32_e32 v186, v186, v250
	v_add_u32_e32 v187, v187, v250
	v_add_u32_e32 v188, v188, v250
	v_add_u32_e32 v189, v189, v250
	v_add_u32_e32 v190, v190, v250
	v_add_u32_e32 v191, v191, v250
	v_add_u32_e32 v192, v192, v250
	v_subrev_u32_e32 v252, s60, v170
	v_subrev_u32_e32 v255, s64, v172
	s_sub_u32 s1, s64, s60
	s_add_i32 s1, s1, 0xffffc000
	v_add_u32_e32 v254, 0x2000, v252
	v_add_u32_e32 v255, s1, v255
	v_add_u32_e32 v201, 0x2000, v255
	s_add_u32 s60, s60, 0xc000
	s_addc_u32 s61, s61, 0
	s_mov_b32 s42, 0x43dc0000
	s_mov_b64 s[54:55], -1
	v_mfma_i32_32x32x32_i8 v[84:99], v[218:221], v[132:135], v[226:241]
	v_mfma_i32_32x32x32_i8 v[84:99], v[222:225], v[136:139], v[84:99]
.Lat_u0:
	ds_read_b128 v[108:111], v193
	ds_read_b128 v[112:115], v193 offset:1024
	v_mfma_i32_32x32x32_i8 v[84:99], v[242:245], v[140:143], v[84:99]
	ds_read_b128 v[116:119], v195 offset:6144
	ds_read_b128 v[120:123], v196 offset:6144
	s_cmp_gt_u32 s43, 29
	s_cbranch_scc1 .Lat_nok0
	s_add_i32 m0, s31, 49152
	ds_read_b128 v[124:127], v195 offset:4096
	global_load_lds_dwordx4 v252, s[60:61]
	s_add_i32 m0, s31, 57344
	v_mfma_i32_32x32x32_i8 v[84:99], v[246:249], v[144:147], v[84:99]
	global_load_lds_dwordx4 v254, s[60:61]
	s_branch .Lat_k0

.Lat_u1:
	ds_read_b128 v[108:111], v193 offset:8192
	ds_read_b128 v[112:115], v193 offset:9216
	v_mfma_i32_32x32x32_i8 v[84:99], v[242:245], v[140:143], v[84:99]
	ds_read_b128 v[116:119], v195 offset:22528
	ds_read_b128 v[120:123], v196 offset:22528
	s_add_i32 m0, s31, 65536
	ds_read_b128 v[124:127], v195 offset:20480
	global_load_lds_dwordx4 v252, s[60:61]
	s_add_i32 m0, s31, 73728
	v_mfma_i32_32x32x32_i8 v[84:99], v[246:249], v[144:147], v[84:99]
	global_load_lds_dwordx4 v254, s[60:61]
	ds_read_b128 v[128:131], v196 offset:20480
	v_mfma_i32_32x32x32_i8 v[84:99], v[202:205], v[148:151], v[84:99]
	ds_read_b128 v[202:205], v195 offset:16384
	v_mfma_i32_32x32x32_i8 v[84:99], v[206:209], v[152:155], v[84:99]
	ds_read_b128 v[206:209], v196 offset:16384
	v_mfma_i32_32x32x32_i8 v[84:99], v[210:213], v[156:159], v[84:99]
	ds_read_b128 v[210:213], v195 offset:18432
	v_mfma_i32_32x32x32_i8 v[84:99], v[214:217], v[160:163], v[84:99]
	ds_read_b128 v[214:217], v196 offset:18432
	v_readlane_b32 s50, v182, s43
	s_waitcnt lgkmcnt(6)
	v_mfma_f32_32x32x64_f8f6f4 v[2:17], v[108:115], v[116:123], v[2:17]
	ds_read_b128 v[218:221], v185
	ds_read_b128 v[222:225], v186
	ds_read_b128 v[242:245], v187
	ds_read_b128 v[246:249], v188
	v_mul_f32_e32 v82, s50, v168
	v_mul_f32_e32 v250, 0x3db8aa3b, v82
	v_fmamk_f32 v251, v250, 0xcb400000, v200
	s_mov_b32 m0, s31
	v_fma_f32 v84, v84, v250, v251
	global_load_lds_dwordx4 v255, s[60:61]
	s_add_i32 m0, s31, 8192
	v_fma_f32 v85, v85, v250, v251
	global_load_lds_dwordx4 v201, s[60:61]
	v_fma_f32 v86, v86, v250, v251
	v_fma_f32 v87, v87, v250, v251
	v_exp_f32_e32 v84, v84
	v_exp_f32_e32 v85, v85
	v_exp_f32_e32 v86, v86
	v_exp_f32_e32 v87, v87
	v_fma_f32 v88, v88, v250, v251
	v_fma_f32 v89, v89, v250, v251
	v_fma_f32 v90, v90, v250, v251
	v_fma_f32 v91, v91, v250, v251
	s_waitcnt lgkmcnt(8)
	v_mfma_f32_32x32x64_f8f6f4 v[18:33], v[108:115], v[124:131], v[18:33]
	v_add_f32_e32 v67, v84, v85
	v_add_f32_e32 v68, v86, v87
	v_exp_f32_e32 v88, v88
	v_exp_f32_e32 v89, v89
	v_exp_f32_e32 v90, v90
	v_exp_f32_e32 v91, v91
	v_add_f32_e32 v67, v67, v68
	v_cvt_pk_fp8_f32 v164, v84, v85
	v_cvt_pk_fp8_f32 v164, v86, v87 op_sel:[0,0,1]
	v_fma_f32 v92, v92, v250, v251
	v_fma_f32 v93, v93, v250, v251
	v_fma_f32 v94, v94, v250, v251
	v_fma_f32 v95, v95, v250, v251
	v_add_f32_e32 v68, v88, v89
	v_add_f32_e32 v69, v90, v91
	s_waitcnt lgkmcnt(6)
	v_mfma_f32_32x32x64_f8f6f4 v[50:65], v[108:115], v[202:209], v[50:65]
	ds_read_b128 v[202:205], v189
	ds_read_b128 v[206:209], v190
	v_exp_f32_e32 v92, v92
	v_exp_f32_e32 v93, v93
	v_exp_f32_e32 v94, v94
	v_exp_f32_e32 v95, v95
	v_add_f32_e32 v68, v68, v69
	v_cvt_pk_fp8_f32 v165, v88, v89
	v_cvt_pk_fp8_f32 v165, v90, v91 op_sel:[0,0,1]
	v_fma_f32 v96, v96, v250, v251
	v_fma_f32 v97, v97, v250, v251
	v_fma_f32 v98, v98, v250, v251
	v_fma_f32 v99, v99, v250, v251
	v_add_f32_e32 v67, v67, v68
	v_add_f32_e32 v68, v92, v93
	v_add_f32_e32 v69, v94, v95
	s_waitcnt lgkmcnt(6)
	v_mfma_f32_32x32x64_f8f6f4 v[34:49], v[108:115], v[210:217], v[34:49]
	ds_read_b128 v[210:213], v191
	ds_read_b128 v[214:217], v192
	v_exp_f32_e32 v96, v96
	v_exp_f32_e32 v97, v97
	v_exp_f32_e32 v98, v98
	v_exp_f32_e32 v99, v99
	v_add_f32_e32 v68, v68, v69
	v_cvt_pk_fp8_f32 v166, v92, v93
	v_cvt_pk_fp8_f32 v166, v94, v95 op_sel:[0,0,1]
	v_add_f32_e32 v67, v67, v68
	v_add_f32_e32 v68, v96, v97
	v_add_f32_e32 v69, v98, v99
	s_add_u32 s60, s60, 0x4000
	s_addc_u32 s61, s61, 0
	v_add_f32_e32 v68, v68, v69
	v_cvt_pk_fp8_f32 v167, v96, v97
	v_cvt_pk_fp8_f32 v167, v98, v99 op_sel:[0,0,1]
	v_add_f32_e32 v67, v67, v68
	ds_write_b128 v194, v[164:167]
	v_cmp_ge_f32_e64 s[52:53], s42, v67
	v_add_f32_e32 v66, v66, v67
	s_add_i32 s43, s43, 1
	s_nop 0
	s_and_b64 s[54:55], s[54:55], s[52:53]
	s_waitcnt lgkmcnt(7)
	v_mfma_i32_32x32x32_i8 v[84:99], v[218:221], v[132:135], v[226:241]
	v_mfma_i32_32x32x32_i8 v[84:99], v[222:225], v[136:139], v[84:99]
	s_waitcnt vmcnt(2) lgkmcnt(0)
	s_barrier
.Lat_u2:
	ds_read_b128 v[108:111], v193
	ds_read_b128 v[112:115], v193 offset:1024
	v_mfma_i32_32x32x32_i8 v[84:99], v[242:245], v[140:143], v[84:99]
	ds_read_b128 v[116:119], v195 offset:38912
	ds_read_b128 v[120:123], v196 offset:38912
	s_add_i32 m0, s31, 81920
	ds_read_b128 v[124:127], v195 offset:36864
	global_load_lds_dwordx4 v252, s[60:61]
	s_add_i32 m0, s31, 90112
	v_mfma_i32_32x32x32_i8 v[84:99], v[246:249], v[144:147], v[84:99]
	global_load_lds_dwordx4 v254, s[60:61]
	ds_read_b128 v[128:131], v196 offset:36864
	v_mfma_i32_32x32x32_i8 v[84:99], v[202:205], v[148:151], v[84:99]
	ds_read_b128 v[202:205], v195 offset:32768
	v_mfma_i32_32x32x32_i8 v[84:99], v[206:209], v[152:155], v[84:99]
	ds_read_b128 v[206:209], v196 offset:32768
	v_mfma_i32_32x32x32_i8 v[84:99], v[210:213], v[156:159], v[84:99]
	ds_read_b128 v[210:213], v195 offset:34816
	v_mfma_i32_32x32x32_i8 v[84:99], v[214:217], v[160:163], v[84:99]
	ds_read_b128 v[214:217], v196 offset:34816
	v_readlane_b32 s50, v182, s43
	s_waitcnt lgkmcnt(6)
	v_mfma_f32_32x32x64_f8f6f4 v[2:17], v[108:115], v[116:123], v[2:17]
	ds_read_b128 v[218:221], v185 offset:16384
	ds_read_b128 v[222:225], v186 offset:16384
	ds_read_b128 v[242:245], v187 offset:16384
	ds_read_b128 v[246:249], v188 offset:16384
	v_mul_f32_e32 v82, s50, v168
	v_mul_f32_e32 v250, 0x3db8aa3b, v82
	v_fmamk_f32 v251, v250, 0xcb400000, v200
	s_add_i32 m0, s31, 16384
	v_fma_f32 v84, v84, v250, v251
	global_load_lds_dwordx4 v255, s[60:61]
	s_add_i32 m0, s31, 24576
	v_fma_f32 v85, v85, v250, v251
	global_load_lds_dwordx4 v201, s[60:61]
	v_fma_f32 v86, v86, v250, v251
	v_fma_f32 v87, v87, v250, v251
	v_exp_f32_e32 v84, v84
	v_exp_f32_e32 v85, v85
	v_exp_f32_e32 v86, v86
	v_exp_f32_e32 v87, v87
	v_fma_f32 v88, v88, v250, v251
	v_fma_f32 v89, v89, v250, v251
	v_fma_f32 v90, v90, v250, v251
	v_fma_f32 v91, v91, v250, v251
	s_waitcnt lgkmcnt(8)
	v_mfma_f32_32x32x64_f8f6f4 v[18:33], v[108:115], v[124:131], v[18:33]
	v_add_f32_e32 v67, v84, v85
	v_add_f32_e32 v68, v86, v87
	v_exp_f32_e32 v88, v88
	v_exp_f32_e32 v89, v89
	v_exp_f32_e32 v90, v90
	v_exp_f32_e32 v91, v91
	v_add_f32_e32 v67, v67, v68
	v_cvt_pk_fp8_f32 v164, v84, v85
	v_cvt_pk_fp8_f32 v164, v86, v87 op_sel:[0,0,1]
	v_fma_f32 v92, v92, v250, v251
	v_fma_f32 v93, v93, v250, v251
	v_fma_f32 v94, v94, v250, v251
	v_fma_f32 v95, v95, v250, v251
	v_add_f32_e32 v68, v88, v89
	v_add_f32_e32 v69, v90, v91
	s_waitcnt lgkmcnt(6)
	v_mfma_f32_32x32x64_f8f6f4 v[50:65], v[108:115], v[202:209], v[50:65]
	ds_read_b128 v[202:205], v189 offset:16384
	ds_read_b128 v[206:209], v190 offset:16384
	v_exp_f32_e32 v92, v92
	v_exp_f32_e32 v93, v93
	v_exp_f32_e32 v94, v94
	v_exp_f32_e32 v95, v95
	v_add_f32_e32 v68, v68, v69
	v_cvt_pk_fp8_f32 v165, v88, v89
	v_cvt_pk_fp8_f32 v165, v90, v91 op_sel:[0,0,1]
	v_fma_f32 v96, v96, v250, v251
	v_fma_f32 v97, v97, v250, v251
	v_fma_f32 v98, v98, v250, v251
	v_fma_f32 v99, v99, v250, v251
	v_add_f32_e32 v67, v67, v68
	v_add_f32_e32 v68, v92, v93
	v_add_f32_e32 v69, v94, v95
	s_waitcnt lgkmcnt(6)
	v_mfma_f32_32x32x64_f8f6f4 v[34:49], v[108:115], v[210:217], v[34:49]
	ds_read_b128 v[210:213], v191 offset:16384
	ds_read_b128 v[214:217], v192 offset:16384
	v_exp_f32_e32 v96, v96
	v_exp_f32_e32 v97, v97
	v_exp_f32_e32 v98, v98
	v_exp_f32_e32 v99, v99
	v_add_f32_e32 v68, v68, v69
	v_cvt_pk_fp8_f32 v166, v92, v93
	v_cvt_pk_fp8_f32 v166, v94, v95 op_sel:[0,0,1]
	v_add_f32_e32 v67, v67, v68
	v_add_f32_e32 v68, v96, v97
	v_add_f32_e32 v69, v98, v99
	s_add_u32 s60, s60, 0x4000
	s_addc_u32 s61, s61, 0
	v_add_f32_e32 v68, v68, v69
	v_cvt_pk_fp8_f32 v167, v96, v97
	v_cvt_pk_fp8_f32 v167, v98, v99 op_sel:[0,0,1]
	v_add_f32_e32 v67, v67, v68
	ds_write_b128 v194, v[164:167] offset:8192
	v_cmp_ge_f32_e64 s[52:53], s42, v67
	v_add_f32_e32 v66, v66, v67
	s_add_i32 s43, s43, 1
	s_nop 0
	s_and_b64 s[54:55], s[54:55], s[52:53]
	s_waitcnt lgkmcnt(7)
	v_mfma_i32_32x32x32_i8 v[84:99], v[218:221], v[132:135], v[226:241]
	v_mfma_i32_32x32x32_i8 v[84:99], v[222:225], v[136:139], v[84:99]
	s_waitcnt vmcnt(2) lgkmcnt(0)
	s_barrier
.Lat_u3:
	ds_read_b128 v[108:111], v193 offset:8192
	ds_read_b128 v[112:115], v193 offset:9216
	v_mfma_i32_32x32x32_i8 v[84:99], v[242:245], v[140:143], v[84:99]
	ds_read_b128 v[116:119], v195 offset:6144
	ds_read_b128 v[120:123], v196 offset:6144
	s_add_i32 m0, s31, 49152
	ds_read_b128 v[124:127], v195 offset:4096
	global_load_lds_dwordx4 v252, s[60:61]
	s_add_i32 m0, s31, 57344
	v_mfma_i32_32x32x32_i8 v[84:99], v[246:249], v[144:147], v[84:99]
	global_load_lds_dwordx4 v254, s[60:61]
	ds_read_b128 v[128:131], v196 offset:4096
	v_mfma_i32_32x32x32_i8 v[84:99], v[202:205], v[148:151], v[84:99]
	ds_read_b128 v[202:205], v195
	v_mfma_i32_32x32x32_i8 v[84:99], v[206:209], v[152:155], v[84:99]
	ds_read_b128 v[206:209], v196
	v_mfma_i32_32x32x32_i8 v[84:99], v[210:213], v[156:159], v[84:99]
	ds_read_b128 v[210:213], v195 offset:2048
	v_mfma_i32_32x32x32_i8 v[84:99], v[214:217], v[160:163], v[84:99]
	ds_read_b128 v[214:217], v196 offset:2048
	v_readlane_b32 s50, v182, s43
	s_waitcnt lgkmcnt(6)
	v_mfma_f32_32x32x64_f8f6f4 v[2:17], v[108:115], v[116:123], v[2:17]
	ds_read_b128 v[218:221], v185 offset:32768
	ds_read_b128 v[222:225], v186 offset:32768
	ds_read_b128 v[242:245], v187 offset:32768
	ds_read_b128 v[246:249], v188 offset:32768
	v_mul_f32_e32 v82, s50, v168
	v_mul_f32_e32 v250, 0x3db8aa3b, v82
	v_fmamk_f32 v251, v250, 0xcb400000, v200
	s_add_i32 m0, s31, 32768
	v_fma_f32 v84, v84, v250, v251
	global_load_lds_dwordx4 v255, s[60:61]
	s_add_i32 m0, s31, 40960
	v_fma_f32 v85, v85, v250, v251
	global_load_lds_dwordx4 v201, s[60:61]
	v_fma_f32 v86, v86, v250, v251
	v_fma_f32 v87, v87, v250, v251
	v_exp_f32_e32 v84, v84
	v_exp_f32_e32 v85, v85
	v_exp_f32_e32 v86, v86
	v_exp_f32_e32 v87, v87
	v_fma_f32 v88, v88, v250, v251
	v_fma_f32 v89, v89, v250, v251
	v_fma_f32 v90, v90, v250, v251
	v_fma_f32 v91, v91, v250, v251
	s_waitcnt lgkmcnt(8)
	v_mfma_f32_32x32x64_f8f6f4 v[18:33], v[108:115], v[124:131], v[18:33]
	v_add_f32_e32 v67, v84, v85
	v_add_f32_e32 v68, v86, v87
	v_exp_f32_e32 v88, v88
	v_exp_f32_e32 v89, v89
	v_exp_f32_e32 v90, v90
	v_exp_f32_e32 v91, v91
	v_add_f32_e32 v67, v67, v68
	v_cvt_pk_fp8_f32 v164, v84, v85
	v_cvt_pk_fp8_f32 v164, v86, v87 op_sel:[0,0,1]
	v_fma_f32 v92, v92, v250, v251
	v_fma_f32 v93, v93, v250, v251
	v_fma_f32 v94, v94, v250, v251
	v_fma_f32 v95, v95, v250, v251
	v_add_f32_e32 v68, v88, v89
	v_add_f32_e32 v69, v90, v91
	s_waitcnt lgkmcnt(6)
	v_mfma_f32_32x32x64_f8f6f4 v[50:65], v[108:115], v[202:209], v[50:65]
	ds_read_b128 v[202:205], v189 offset:32768
	ds_read_b128 v[206:209], v190 offset:32768
	v_exp_f32_e32 v92, v92
	v_exp_f32_e32 v93, v93
	v_exp_f32_e32 v94, v94
	v_exp_f32_e32 v95, v95
	v_add_f32_e32 v68, v68, v69
	v_cvt_pk_fp8_f32 v165, v88, v89
	v_cvt_pk_fp8_f32 v165, v90, v91 op_sel:[0,0,1]
	v_fma_f32 v96, v96, v250, v251
	v_fma_f32 v97, v97, v250, v251
	v_fma_f32 v98, v98, v250, v251
	v_fma_f32 v99, v99, v250, v251
	v_add_f32_e32 v67, v67, v68
	v_add_f32_e32 v68, v92, v93
	v_add_f32_e32 v69, v94, v95
	s_waitcnt lgkmcnt(6)
	v_mfma_f32_32x32x64_f8f6f4 v[34:49], v[108:115], v[210:217], v[34:49]
	ds_read_b128 v[210:213], v191 offset:32768
	ds_read_b128 v[214:217], v192 offset:32768
	v_exp_f32_e32 v96, v96
	v_exp_f32_e32 v97, v97
	v_exp_f32_e32 v98, v98
	v_exp_f32_e32 v99, v99
	v_add_f32_e32 v68, v68, v69
	v_cvt_pk_fp8_f32 v166, v92, v93
	v_cvt_pk_fp8_f32 v166, v94, v95 op_sel:[0,0,1]
	v_add_f32_e32 v67, v67, v68
	v_add_f32_e32 v68, v96, v97
	v_add_f32_e32 v69, v98, v99
	s_add_u32 s60, s60, 0x4000
	s_addc_u32 s61, s61, 0
	v_add_f32_e32 v68, v68, v69
	v_cvt_pk_fp8_f32 v167, v96, v97
	v_cvt_pk_fp8_f32 v167, v98, v99 op_sel:[0,0,1]
	v_add_f32_e32 v67, v67, v68
	ds_write_b128 v194, v[164:167]
	v_cmp_ge_f32_e64 s[52:53], s42, v67
	v_add_f32_e32 v66, v66, v67
	s_add_i32 s43, s43, 1
	s_nop 0
	s_and_b64 s[54:55], s[54:55], s[52:53]
	s_waitcnt lgkmcnt(7)
	v_mfma_i32_32x32x32_i8 v[84:99], v[218:221], v[132:135], v[226:241]
	v_mfma_i32_32x32x32_i8 v[84:99], v[222:225], v[136:139], v[84:99]
	s_waitcnt vmcnt(2) lgkmcnt(0)
	s_barrier
.Lat_u4:
	ds_read_b128 v[108:111], v193
	ds_read_b128 v[112:115], v193 offset:1024
	v_mfma_i32_32x32x32_i8 v[84:99], v[242:245], v[140:143], v[84:99]
	ds_read_b128 v[116:119], v195 offset:22528
	ds_read_b128 v[120:123], v196 offset:22528
	s_add_i32 m0, s31, 65536
	ds_read_b128 v[124:127], v195 offset:20480
	global_load_lds_dwordx4 v252, s[60:61]
	s_add_i32 m0, s31, 73728
	v_mfma_i32_32x32x32_i8 v[84:99], v[246:249], v[144:147], v[84:99]
	global_load_lds_dwordx4 v254, s[60:61]
	ds_read_b128 v[128:131], v196 offset:20480
	v_mfma_i32_32x32x32_i8 v[84:99], v[202:205], v[148:151], v[84:99]
	ds_read_b128 v[202:205], v195 offset:16384
	v_mfma_i32_32x32x32_i8 v[84:99], v[206:209], v[152:155], v[84:99]
	ds_read_b128 v[206:209], v196 offset:16384
	v_mfma_i32_32x32x32_i8 v[84:99], v[210:213], v[156:159], v[84:99]
	ds_read_b128 v[210:213], v195 offset:18432
	v_mfma_i32_32x32x32_i8 v[84:99], v[214:217], v[160:163], v[84:99]
	ds_read_b128 v[214:217], v196 offset:18432
	v_readlane_b32 s50, v182, s43
	s_waitcnt lgkmcnt(6)
	v_mfma_f32_32x32x64_f8f6f4 v[2:17], v[108:115], v[116:123], v[2:17]
	ds_read_b128 v[218:221], v185
	ds_read_b128 v[222:225], v186
	ds_read_b128 v[242:245], v187
	ds_read_b128 v[246:249], v188
	v_mul_f32_e32 v82, s50, v168
	v_mul_f32_e32 v250, 0x3db8aa3b, v82
	v_fmamk_f32 v251, v250, 0xcb400000, v200
	s_mov_b32 m0, s31
	v_fma_f32 v84, v84, v250, v251
	global_load_lds_dwordx4 v255, s[60:61]
	s_add_i32 m0, s31, 8192
	v_fma_f32 v85, v85, v250, v251
	global_load_lds_dwordx4 v201, s[60:61]
	v_fma_f32 v86, v86, v250, v251
	v_fma_f32 v87, v87, v250, v251
	v_exp_f32_e32 v84, v84
	v_exp_f32_e32 v85, v85
	v_exp_f32_e32 v86, v86
	v_exp_f32_e32 v87, v87
	v_fma_f32 v88, v88, v250, v251
	v_fma_f32 v89, v89, v250, v251
	v_fma_f32 v90, v90, v250, v251
	v_fma_f32 v91, v91, v250, v251
	s_waitcnt lgkmcnt(8)
	v_mfma_f32_32x32x64_f8f6f4 v[18:33], v[108:115], v[124:131], v[18:33]
	v_add_f32_e32 v67, v84, v85
	v_add_f32_e32 v68, v86, v87
	v_exp_f32_e32 v88, v88
	v_exp_f32_e32 v89, v89
	v_exp_f32_e32 v90, v90
	v_exp_f32_e32 v91, v91
	v_add_f32_e32 v67, v67, v68
	v_cvt_pk_fp8_f32 v164, v84, v85
	v_cvt_pk_fp8_f32 v164, v86, v87 op_sel:[0,0,1]
	v_fma_f32 v92, v92, v250, v251
	v_fma_f32 v93, v93, v250, v251
	v_fma_f32 v94, v94, v250, v251
	v_fma_f32 v95, v95, v250, v251
	v_add_f32_e32 v68, v88, v89
	v_add_f32_e32 v69, v90, v91
	s_waitcnt lgkmcnt(6)
	v_mfma_f32_32x32x64_f8f6f4 v[50:65], v[108:115], v[202:209], v[50:65]
	ds_read_b128 v[202:205], v189
	ds_read_b128 v[206:209], v190
	v_exp_f32_e32 v92, v92
	v_exp_f32_e32 v93, v93
	v_exp_f32_e32 v94, v94
	v_exp_f32_e32 v95, v95
	v_add_f32_e32 v68, v68, v69
	v_cvt_pk_fp8_f32 v165, v88, v89
	v_cvt_pk_fp8_f32 v165, v90, v91 op_sel:[0,0,1]
	v_fma_f32 v96, v96, v250, v251
	v_fma_f32 v97, v97, v250, v251
	v_fma_f32 v98, v98, v250, v251
	v_fma_f32 v99, v99, v250, v251
	v_add_f32_e32 v67, v67, v68
	v_add_f32_e32 v68, v92, v93
	v_add_f32_e32 v69, v94, v95
	s_waitcnt lgkmcnt(6)
	v_mfma_f32_32x32x64_f8f6f4 v[34:49], v[108:115], v[210:217], v[34:49]
	ds_read_b128 v[210:213], v191
	ds_read_b128 v[214:217], v192
	v_exp_f32_e32 v96, v96
	v_exp_f32_e32 v97, v97
	v_exp_f32_e32 v98, v98
	v_exp_f32_e32 v99, v99
	v_add_f32_e32 v68, v68, v69
	v_cvt_pk_fp8_f32 v166, v92, v93
	v_cvt_pk_fp8_f32 v166, v94, v95 op_sel:[0,0,1]
	v_add_f32_e32 v67, v67, v68
	v_add_f32_e32 v68, v96, v97
	v_add_f32_e32 v69, v98, v99
	s_add_u32 s60, s60, 0x4000
	s_addc_u32 s61, s61, 0
	v_add_f32_e32 v68, v68, v69
	v_cvt_pk_fp8_f32 v167, v96, v97
	v_cvt_pk_fp8_f32 v167, v98, v99 op_sel:[0,0,1]
	v_add_f32_e32 v67, v67, v68
	ds_write_b128 v194, v[164:167] offset:8192
	v_cmp_ge_f32_e64 s[52:53], s42, v67
	v_add_f32_e32 v66, v66, v67
	s_add_i32 s43, s43, 1
	s_nop 0
	s_and_b64 s[54:55], s[54:55], s[52:53]
	s_waitcnt lgkmcnt(7)
	v_mfma_i32_32x32x32_i8 v[84:99], v[218:221], v[132:135], v[226:241]
	v_mfma_i32_32x32x32_i8 v[84:99], v[222:225], v[136:139], v[84:99]
	s_waitcnt vmcnt(2) lgkmcnt(0)
	s_barrier
.Lat_u5:
	ds_read_b128 v[108:111], v193 offset:8192
	ds_read_b128 v[112:115], v193 offset:9216
	v_mfma_i32_32x32x32_i8 v[84:99], v[242:245], v[140:143], v[84:99]
	ds_read_b128 v[116:119], v195 offset:38912
	ds_read_b128 v[120:123], v196 offset:38912
	s_cmp_gt_u32 s43, 29
	s_cbranch_scc1 .Lat_nok5
	s_add_i32 m0, s31, 81920
	ds_read_b128 v[124:127], v195 offset:36864
	global_load_lds_dwordx4 v252, s[60:61]
	s_add_i32 m0, s31, 90112
	v_mfma_i32_32x32x32_i8 v[84:99], v[246:249], v[144:147], v[84:99]
	global_load_lds_dwordx4 v254, s[60:61]
	s_branch .Lat_k5

.LBB2_16:
	v_add_u32_e32 v110, 0, v195
	v_add_u32_e32 v118, 0, v196
	ds_read_b128 v[82:85], v193 offset:8192
	ds_read_b128 v[86:89], v193 offset:9216
	ds_read_b128 v[90:93], v110 offset:16384
	ds_read_b128 v[98:101], v110 offset:18432
	ds_read_b128 v[94:97], v118 offset:16384
	ds_read_b128 v[102:105], v118 offset:18432
	ds_read_b128 v[106:109], v110 offset:20480
	ds_read_b128 v[114:117], v110 offset:22528
	ds_read_b128 v[110:113], v118 offset:20480
	ds_read_b128 v[118:121], v118 offset:22528
	s_waitcnt lgkmcnt(0)
	v_mfma_f32_32x32x64_f8f6f4 v[50:65], v[82:89], v[90:97], v[50:65]
	s_cmp_lg_u32 s39, 0
	s_cselect_b64 s[0:1], -1, 0
	v_cmp_eq_u32_e32 vcc, 0, v198
	s_and_b64 s[6:7], vcc, s[0:1]
	v_mfma_f32_32x32x64_f8f6f4 v[34:49], v[82:89], v[98:105], v[34:49]
	v_mfma_f32_32x32x64_f8f6f4 v[18:33], v[82:89], v[106:113], v[18:33]
	v_mfma_f32_32x32x64_f8f6f4 v[2:17], v[82:89], v[114:121], v[2:17]
	s_and_saveexec_b64 s[0:1], s[6:7]
	s_add_i32 s6, 0, 0x1cc00
	v_mov_b32_e32 v82, 1
	v_mov_b32_e32 v83, s6
	ds_write_b32 v83, v82
	s_or_b64 exec, exec, s[0:1]
	s_add_i32 s0, 0, 0x1cc00
	v_mov_b32_e32 v82, s0
	s_waitcnt vmcnt(0) lgkmcnt(0)
	s_barrier
	ds_read_b32 v82, v82
	s_waitcnt lgkmcnt(0)
	v_cmp_eq_u32_e32 vcc, 0, v82
	s_cbranch_vccnz .Lat_lsum
	s_mov_b32 m0, s36
	s_barrier
	global_load_lds_dwordx4 v[174:175], off
	s_mov_b32 m0, s35
	s_lshl_b32 s0, s34, 5
	global_load_lds_dwordx4 v[176:177], off
	s_mov_b32 m0, s31
	s_lshl_b32 s1, s34, 7
	global_load_lds_dwordx4 v[178:179], off
	s_mov_b32 m0, s37
	s_add_i32 s1, s1, 0
	global_load_lds_dwordx4 v[180:181], off
	v_or_b32_e32 v2, s0, v1
	s_add_i32 s1, s1, 0x1c400
	v_bitop3_b32 v4, s0, 32, v1 bitop3:0x36
	v_lshlrev_b32_e32 v2, 2, v2
	v_add_u32_e32 v3, s1, v199
	v_lshlrev_b32_e32 v5, 4, v183
	v_lshlrev_b32_e32 v4, 2, v4
	v_add3_u32 v120, s38, v2, v199
	v_mov_b32_e32 v2, 0
	s_mov_b32 s20, 0
	v_lshl_add_u32 v118, v1, 2, v3
	v_add3_u32 v119, s38, v4, v199
	v_mov_b32_e32 v101, 0xf149f2ca
	s_mov_b64 s[0:1], 0
	s_mov_b64 s[6:7], 0x4000
	s_mov_b64 s[8:9], 0x6000
	v_add_u32_e32 v121, v3, v5
	s_mov_b32 s21, 0xbdb8aa3b
	v_mov_b32_e32 v82, 0x4b400000
	v_mov_b32_e32 v100, 0x38383838
	v_mov_b32_e32 v3, v2
	v_mov_b32_e32 v4, v2
	v_mov_b32_e32 v5, v2
	v_mov_b32_e32 v6, v2
	v_mov_b32_e32 v7, v2
	v_mov_b32_e32 v8, v2
	v_mov_b32_e32 v9, v2
	v_mov_b32_e32 v10, v2
	v_mov_b32_e32 v11, v2
	v_mov_b32_e32 v12, v2
	v_mov_b32_e32 v13, v2
	v_mov_b32_e32 v14, v2
	v_mov_b32_e32 v15, v2
	v_mov_b32_e32 v16, v2
	v_mov_b32_e32 v17, v2
	v_mov_b32_e32 v18, v2
	v_mov_b32_e32 v19, v2
	v_mov_b32_e32 v20, v2
	v_mov_b32_e32 v21, v2
	v_mov_b32_e32 v22, v2
	v_mov_b32_e32 v23, v2
	v_mov_b32_e32 v24, v2
	v_mov_b32_e32 v25, v2
	v_mov_b32_e32 v26, v2
	v_mov_b32_e32 v27, v2
	v_mov_b32_e32 v28, v2
	v_mov_b32_e32 v29, v2
	v_mov_b32_e32 v30, v2
	v_mov_b32_e32 v31, v2
	v_mov_b32_e32 v32, v2
	v_mov_b32_e32 v33, v2
	v_mov_b32_e32 v34, v2
	v_mov_b32_e32 v35, v2
	v_mov_b32_e32 v36, v2
	v_mov_b32_e32 v37, v2
	v_mov_b32_e32 v38, v2
	v_mov_b32_e32 v39, v2
	v_mov_b32_e32 v40, v2
	v_mov_b32_e32 v41, v2
	v_mov_b32_e32 v42, v2
	v_mov_b32_e32 v43, v2
	v_mov_b32_e32 v44, v2
	v_mov_b32_e32 v45, v2
	v_mov_b32_e32 v46, v2
	v_mov_b32_e32 v47, v2
	v_mov_b32_e32 v48, v2
	v_mov_b32_e32 v49, v2
	v_mov_b32_e32 v50, v2
	v_mov_b32_e32 v51, v2
	v_mov_b32_e32 v52, v2
	v_mov_b32_e32 v53, v2
	v_mov_b32_e32 v54, v2
	v_mov_b32_e32 v55, v2
	v_mov_b32_e32 v56, v2
	v_mov_b32_e32 v57, v2
	v_mov_b32_e32 v58, v2
	v_mov_b32_e32 v59, v2
	v_mov_b32_e32 v60, v2
	v_mov_b32_e32 v61, v2
	v_mov_b32_e32 v62, v2
	v_mov_b32_e32 v63, v2
	v_mov_b32_e32 v64, v2
	v_mov_b32_e32 v65, v2
	v_mov_b32_e32 v66, v2
	v_mov_b32_e32 v67, v2
	v_mov_b32_e32 v68, v2
	v_mov_b32_e32 v69, v2
	v_mov_b32_e32 v70, v2
	v_mov_b32_e32 v71, v2
	v_mov_b32_e32 v72, v2
	v_mov_b32_e32 v73, v2
	v_mov_b32_e32 v74, v2
	v_mov_b32_e32 v75, v2
	v_mov_b32_e32 v76, v2
	v_mov_b32_e32 v77, v2
	v_mov_b32_e32 v78, v2
	v_mov_b32_e32 v79, v2
	v_mov_b32_e32 v80, v2
	v_mov_b32_e32 v81, v2
	s_waitcnt vmcnt(0) lgkmcnt(0)
	s_barrier
	s_cmp_eq_u32 s0, 0x7c000
	s_movk_i32 s22, 0x4000
	s_cbranch_scc1 .LBB2_21

.LBB2_25:
	s_or_b64 exec, exec, s[18:19]
	s_waitcnt lgkmcnt(0)
	v_mul_f32_e32 v83, 0x3db8aa3b, v83
	v_fma_f32 v101, v197, s21, 2.0
	ds_read_b128 v[114:117], v121 offset:96
	ds_read_b128 v[110:113], v121 offset:64
	ds_read_b128 v[106:109], v121 offset:32
	ds_read_b128 v[102:105], v121
	v_fmac_f32_e32 v101, 0xcb400000, v83
	v_fma_f32 v84, v84, v83, v101
	s_waitcnt lgkmcnt(3)
	v_pk_mul_f32 v[78:79], v[78:79], v[114:115]
	v_pk_mul_f32 v[62:63], v[114:115], v[62:63]
	v_pk_mul_f32 v[46:47], v[114:115], v[46:47]
	v_pk_mul_f32 v[30:31], v[114:115], v[30:31]
	v_pk_mul_f32 v[14:15], v[114:115], v[14:15]
	v_exp_f32_e32 v114, v84
	v_fma_f32 v84, v85, v83, v101
	v_exp_f32_e32 v85, v84
	v_fma_f32 v84, v86, v83, v101
	v_exp_f32_e32 v115, v84
	v_fma_f32 v84, v87, v83, v101
	v_exp_f32_e32 v122, v84
	v_fma_f32 v84, v88, v83, v101
	v_exp_f32_e32 v86, v84
	v_fma_f32 v84, v89, v83, v101
	v_exp_f32_e32 v87, v84
	v_fma_f32 v84, v90, v83, v101
	v_exp_f32_e32 v88, v84
	v_fma_f32 v84, v91, v83, v101
	v_exp_f32_e32 v89, v84
	v_fma_f32 v84, v92, v83, v101
	v_exp_f32_e32 v90, v84
	v_fma_f32 v84, v93, v83, v101
	v_exp_f32_e32 v91, v84
	v_fma_f32 v84, v94, v83, v101
	v_exp_f32_e32 v92, v84
	v_fma_f32 v84, v95, v83, v101
	v_exp_f32_e32 v93, v84
	v_fma_f32 v84, v96, v83, v101
	v_exp_f32_e32 v94, v84
	v_fma_f32 v84, v97, v83, v101
	v_exp_f32_e32 v95, v84
	v_fma_f32 v84, v98, v83, v101
	v_exp_f32_e32 v96, v84
	v_mov_b32_e32 v84, 0
	v_cvt_pk_fp8_f32 v84, v114, v85
	v_mov_b32_e32 v85, 0
	v_fmac_f32_e32 v101, v99, v83
	v_cvt_pk_fp8_f32 v85, v86, v87
	v_mov_b32_e32 v86, 0
	v_mov_b32_e32 v87, 0
	v_exp_f32_e32 v83, v101
	v_cvt_pk_fp8_f32 v86, v90, v91
	v_cvt_pk_fp8_f32 v87, v94, v95
	v_cvt_pk_fp8_f32 v84, v115, v122 op_sel:[0,0,1]
	v_cvt_pk_fp8_f32 v85, v88, v89 op_sel:[0,0,1]
	v_cvt_pk_fp8_f32 v86, v92, v93 op_sel:[0,0,1]
	v_cvt_pk_fp8_f32 v87, v96, v83 op_sel:[0,0,1]
	s_add_i32 s18, s22, 0
	v_add_u32_e32 v83, s18, v195
	v_add_u32_e32 v101, s18, v196
	ds_write_b128 v194, v[84:87]
	s_waitcnt lgkmcnt(0)
	s_barrier
	ds_read_b128 v[84:87], v193
	ds_read_b128 v[88:91], v193 offset:1024
	ds_read_b128 v[92:95], v83
	ds_read_b128 v[122:125], v83 offset:2048
	ds_read_b128 v[96:99], v101
	ds_read_b128 v[126:129], v101 offset:2048
	ds_read_b128 v[174:177], v83 offset:4096
	ds_read_b128 v[198:201], v83 offset:6144
	ds_read_b128 v[178:181], v101 offset:4096
	ds_read_b128 v[202:205], v101 offset:6144
	v_pk_mul_f32 v[74:75], v[74:75], v[110:111]
	v_pk_mul_f32 v[70:71], v[70:71], v[106:107]
	v_pk_mul_f32 v[66:67], v[66:67], v[102:103]
	v_pk_mul_f32 v[80:81], v[80:81], v[116:117]
	v_pk_mul_f32 v[76:77], v[76:77], v[112:113]
	v_pk_mul_f32 v[72:73], v[72:73], v[108:109]
	v_pk_mul_f32 v[68:69], v[68:69], v[104:105]
	v_pk_mul_f32 v[58:59], v[110:111], v[58:59]
	v_pk_mul_f32 v[54:55], v[106:107], v[54:55]
	v_pk_mul_f32 v[50:51], v[102:103], v[50:51]
	v_pk_mul_f32 v[64:65], v[116:117], v[64:65]
	v_pk_mul_f32 v[60:61], v[112:113], v[60:61]
	v_pk_mul_f32 v[56:57], v[108:109], v[56:57]
	v_pk_mul_f32 v[52:53], v[104:105], v[52:53]
	v_pk_mul_f32 v[42:43], v[110:111], v[42:43]
	v_pk_mul_f32 v[38:39], v[106:107], v[38:39]
	v_pk_mul_f32 v[34:35], v[102:103], v[34:35]
	v_pk_mul_f32 v[48:49], v[116:117], v[48:49]
	v_pk_mul_f32 v[44:45], v[112:113], v[44:45]
	v_pk_mul_f32 v[40:41], v[108:109], v[40:41]
	v_pk_mul_f32 v[36:37], v[104:105], v[36:37]
	v_pk_mul_f32 v[26:27], v[110:111], v[26:27]
	v_pk_mul_f32 v[22:23], v[106:107], v[22:23]
	v_pk_mul_f32 v[18:19], v[102:103], v[18:19]
	v_pk_mul_f32 v[32:33], v[116:117], v[32:33]
	v_pk_mul_f32 v[28:29], v[112:113], v[28:29]
	v_pk_mul_f32 v[24:25], v[108:109], v[24:25]
	v_pk_mul_f32 v[20:21], v[104:105], v[20:21]
	v_pk_mul_f32 v[10:11], v[110:111], v[10:11]
	v_pk_mul_f32 v[6:7], v[106:107], v[6:7]
	v_pk_mul_f32 v[2:3], v[102:103], v[2:3]
	v_pk_mul_f32 v[16:17], v[116:117], v[16:17]
	v_pk_mul_f32 v[12:13], v[112:113], v[12:13]
	v_pk_mul_f32 v[8:9], v[108:109], v[8:9]
	v_pk_mul_f32 v[4:5], v[104:105], v[4:5]
	v_mov_b32_e32 v101, v100
	v_mov_b32_e32 v102, v100
	v_mov_b32_e32 v103, v100
	v_mov_b32_e32 v104, v100
	v_mov_b32_e32 v105, v100
	v_mov_b32_e32 v106, v100
	v_mov_b32_e32 v107, v100
	s_waitcnt lgkmcnt(5)
	v_mfma_f32_32x32x64_f8f6f4 v[50:65], v[84:91], v[92:99], v[50:65]
	s_add_u32 s0, s0, 0x4000
	s_addc_u32 s1, s1, 0
	s_add_i32 s20, s20, 1
	s_cmp_lg_u32 s0, 0x80000
	s_waitcnt lgkmcnt(0)
	s_barrier
	v_mfma_f32_32x32x64_f8f6f4 v[34:49], v[84:91], v[122:129], v[34:49]
	v_mfma_f32_32x32x64_f8f6f4 v[18:33], v[84:91], v[174:181], v[18:33]
	v_mfma_f32_32x32x64_f8f6f4 v[2:17], v[84:91], v[198:205], v[2:17]
	v_mfma_f32_32x32x64_f8f6f4 v[66:81], v[84:91], v[100:107], v[66:81]
	s_cbranch_scc0 .LBB2_27
	v_mov_b32_e32 v101, v197
	s_cmp_eq_u32 s0, 0x7c000
	s_movk_i32 s22, 0x4000
	s_cbranch_scc0 .LBB2_20
	s_branch .LBB2_21
